# v21 + nt on P1's read-once x/ctx row loads
# baseline (speedup 1.0000x reference)
; __device__ __forceinline__ void p1_ln_mod(Frame& F) {
;     ...
;     for (int m = gw; m < MTOT; m += NGW) {
;         const int b = m / RPB, idx = m % RPB; const float* src; const float* md;
;         if (idx < SEQ) { src = F.in[I_X] + (size_t)(b * SEQ + idx) * DM; md = mod + (size_t)b * 12288; } else { src = F.in[I_CTX] + (size_t)(b * CTXL + idx - SEQ) * DM; md = mod + 2 * 12288; }
;         const f32x4* xr = (const f32x4*)src + F.lane; f32x4 v[8]; float s = 0.f;
; #pragma unroll
;         for (int j = 0; j < 8; ++j) { v[j] = xr[64 * j]; s += (v[j][0] + v[j][1]) + (v[j][2] + v[j][3]); }
;         const float mean = wave_sum(s) * (1.f / DM); float s2 = 0.f;
; #pragma unroll
;         for (int j = 0; j < 8; ++j) { v[j] = v[j] - mean; s2 += (v[j][0] * v[j][0] + v[j][1] * v[j][1]) + (v[j][2] * v[j][2] + v[j][3] * v[j][3]); }
;         const float rstd = 1.f / sqrtf(wave_sum(s2) * (1.f / DM) + LN_EPS);
.LBB0_189:
	global_load_dwordx4 v[30:33], v34, s[0:1] nt
	global_load_dwordx4 v[26:29], v34, s[0:1] offset:1024 nt
	global_load_dwordx4 v[22:25], v34, s[0:1] offset:2048 nt
	global_load_dwordx4 v[18:21], v34, s[0:1] offset:3072 nt
	v_lshl_add_u64 v[2:3], s[0:1], 0, v[34:35]
	v_add_co_u32_e32 v2, vcc, s42, v2
	s_ashr_i32 s13, s12, 31
	s_nop 0
	v_addc_co_u32_e32 v3, vcc, 0, v3, vcc
	global_load_dwordx4 v[14:17], v[2:3], off nt
	global_load_dwordx4 v[10:13], v[2:3], off offset:1024 nt
	global_load_dwordx4 v[6:9], v[2:3], off offset:2048 nt
	s_nop 0
	global_load_dwordx4 v[2:5], v[2:3], off offset:3072 nt
	s_lshl_b64 s[38:39], s[12:13], 11
	s_lshl_b64 s[0:1], s[12:13], 12
	s_add_u32 s24, s20, 0x2000
	s_addc_u32 s25, s21, 0
	s_add_i32 s12, s12, s3
	s_cmpk_lt_i32 s12, 0x2200
	s_waitcnt vmcnt(7)
	v_mov_b32_e32 v56, v30
	s_waitcnt vmcnt(6)
	v_mov_b32_e32 v57, v26
	v_mov_b32_e32 v58, v31
	v_mov_b32_e32 v59, v27
	v_mov_b32_e32 v60, v32
	v_mov_b32_e32 v61, v28
	v_mov_b32_e32 v62, v33
	v_mov_b32_e32 v63, v29
	s_waitcnt vmcnt(5)
	v_mov_b32_e32 v64, v23
	v_mov_b32_e32 v65, v24
	v_mov_b32_e32 v66, v22
	v_mov_b32_e32 v67, v25
	v_pk_add_f32 v[56:57], v[56:57], v[58:59]
	v_pk_add_f32 v[58:59], v[60:61], v[62:63]
	v_pk_add_f32 v[60:61], v[64:65], v[66:67]
	v_pk_add_f32 v[56:57], v[56:57], v[58:59]
	v_pk_add_f32 v[58:59], v[60:61], v[60:61] op_sel:[0,1] op_sel_hi:[1,0]
	v_add_f32_e32 v56, 0, v56
	s_waitcnt vmcnt(4)
	v_add_f32_e32 v68, v18, v19
	v_add_f32_e32 v70, v20, v21
	s_waitcnt vmcnt(3)
	v_mov_b32_e32 v61, v14
	v_mov_b32_e32 v69, v16
	v_mov_b32_e32 v71, v17
	v_mov_b32_e32 v59, v15
	v_add_f32_e32 v60, v56, v57
	s_waitcnt vmcnt(2)
	v_mov_b32_e32 v62, v11
	v_mov_b32_e32 v63, v12
	v_mov_b32_e32 v64, v10
	v_mov_b32_e32 v65, v13
	v_pk_add_f32 v[68:69], v[68:69], v[70:71]
	v_pk_add_f32 v[58:59], v[60:61], v[58:59]
	v_pk_add_f32 v[62:63], v[62:63], v[64:65]
	v_pk_add_f32 v[58:59], v[58:59], v[68:69]
	v_pk_add_f32 v[56:57], v[62:63], v[62:63] op_sel:[0,1] op_sel_hi:[1,0]
	v_pk_add_f32 v[58:59], v[58:59], v[58:59] op_sel:[0,1] op_sel_hi:[1,0]
	s_waitcnt vmcnt(1)
	v_add_f32_e32 v66, v6, v7
	v_add_f32_e32 v72, v8, v9
	s_waitcnt vmcnt(0)
	v_mov_b32_e32 v67, v4
	v_mov_b32_e32 v73, v5
	v_mov_b32_e32 v57, v3
	v_mov_b32_e32 v59, v2
	v_pk_add_f32 v[64:65], v[66:67], v[72:73]
	v_pk_add_f32 v[56:57], v[58:59], v[56:57]
	s_nop 0
	v_pk_add_f32 v[56:57], v[56:57], v[64:65]
	s_nop 0
	v_add_f32_e32 v56, v56, v57
	ds_bpermute_b32 v57, v1, v56
	s_waitcnt lgkmcnt(0)
	v_add_f32_e32 v56, v56, v57
	ds_bpermute_b32 v57, v42, v56
	s_waitcnt lgkmcnt(0)
	v_add_f32_e32 v56, v56, v57
	ds_bpermute_b32 v57, v43, v56
	s_waitcnt lgkmcnt(0)
	v_add_f32_e32 v56, v56, v57
	ds_bpermute_b32 v57, v44, v56
	s_waitcnt lgkmcnt(0)
	v_add_f32_e32 v56, v56, v57
	ds_bpermute_b32 v57, v45, v56
	s_waitcnt lgkmcnt(0)
	v_add_f32_e32 v56, v56, v57
	ds_bpermute_b32 v57, v46, v56
	s_waitcnt lgkmcnt(0)
	v_add_f32_e32 v78, v56, v57
	v_fmamk_f32 v33, v78, 0xba000000, v33
	v_fmamk_f32 v31, v78, 0xba000000, v31
	v_fmamk_f32 v65, v78, 0xba000000, v29
	v_fmamk_f32 v27, v78, 0xba000000, v27
	v_fmamk_f32 v67, v78, 0xba000000, v23
	v_fmamk_f32 v66, v78, 0xba000000, v22
	v_fmamk_f32 v25, v78, 0xba000000, v25
	v_fmac_f32_e32 v24, 0xba000000, v78
	v_fmamk_f32 v68, v78, 0xba000000, v18
	v_fmac_f32_e32 v20, 0xba000000, v78
	v_fmamk_f32 v11, v78, 0xba000000, v11
	v_fmamk_f32 v10, v78, 0xba000000, v10
	v_fmamk_f32 v13, v78, 0xba000000, v13
	v_fmac_f32_e32 v12, 0xba000000, v78
	v_fmamk_f32 v32, v78, 0xba000000, v32
	v_fmac_f32_e32 v30, 0xba000000, v78
	v_fmamk_f32 v64, v78, 0xba000000, v28
	v_fmac_f32_e32 v26, 0xba000000, v78
	v_fmamk_f32 v69, v78, 0xba000000, v19
	v_fmamk_f32 v21, v78, 0xba000000, v21
	v_mov_b32_e32 v22, v31
	v_mov_b32_e32 v23, v27
	v_mov_b32_e32 v56, v33
	v_mov_b32_e32 v57, v65
	v_pk_mul_f32 v[58:59], v[24:25], v[24:25]
	v_pk_mul_f32 v[60:61], v[66:67], v[66:67]
	v_mul_f32_e32 v62, v68, v68
	v_mul_f32_e32 v70, v20, v20
	v_pk_mul_f32 v[72:73], v[12:13], v[12:13]
	v_pk_mul_f32 v[74:75], v[10:11], v[10:11]
	v_fmamk_f32 v19, v78, 0xba000000, v17
	v_fmamk_f32 v18, v78, 0xba000000, v16
	v_fmamk_f32 v15, v78, 0xba000000, v15
	v_fmac_f32_e32 v14, 0xba000000, v78
	v_mov_b32_e32 v16, v30
	v_mov_b32_e32 v17, v26
	v_mov_b32_e32 v28, v32
	v_mov_b32_e32 v29, v64
	v_pk_mul_f32 v[22:23], v[22:23], v[22:23]
	v_pk_mul_f32 v[56:57], v[56:57], v[56:57]
	v_pk_mov_b32 v[76:77], v[60:61], v[58:59] op_sel:[1,0]
	v_mov_b32_e32 v61, v59
	v_pk_fma_f32 v[58:59], v[68:69], v[68:69], v[62:63] op_sel_hi:[1,1,0]
	v_pk_fma_f32 v[62:63], v[20:21], v[20:21], v[70:71] op_sel_hi:[1,1,0]
	v_pk_mov_b32 v[70:71], v[74:75], v[72:73] op_sel:[1,0]
	v_mov_b32_e32 v75, v73
	v_pk_fma_f32 v[16:17], v[16:17], v[16:17], v[22:23]
	v_pk_fma_f32 v[22:23], v[28:29], v[28:29], v[56:57]
	v_pk_add_f32 v[28:29], v[76:77], v[60:61]
	v_mul_f32_e32 v58, v14, v14
	v_mul_f32_e32 v62, v15, v15
	v_pk_add_f32 v[56:57], v[70:71], v[74:75]
	v_pk_add_f32 v[16:17], v[16:17], v[22:23]
	v_pk_add_f32 v[22:23], v[28:29], v[28:29] op_sel_hi:[0,1]
	v_pk_add_f32 v[28:29], v[58:59], v[62:63]
	v_pk_add_f32 v[70:71], v[56:57], v[56:57] op_sel_hi:[0,1]
	global_load_dwordx4 v[56:59], v34, s[20:21]
	global_load_dwordx4 v[60:63], v34, s[24:25]
	v_pk_add_f32 v[16:17], v[16:17], v[16:17] op_sel_hi:[0,1]
	v_mul_f32_e32 v22, v18, v18
	v_mul_f32_e32 v16, v19, v19
	v_pk_add_f32 v[16:17], v[22:23], v[16:17]
	v_fmac_f32_e32 v8, 0xba000000, v78
	v_pk_add_f32 v[16:17], v[28:29], v[16:17]
	v_fmamk_f32 v9, v78, 0xba000000, v9
	v_pk_add_f32 v[22:23], v[16:17], v[16:17] op_sel_hi:[0,1]
	v_fmamk_f32 v16, v78, 0xba000000, v6
	v_fmamk_f32 v17, v78, 0xba000000, v7
	v_mul_f32_e32 v6, v16, v16
	v_pk_fma_f32 v[6:7], v[16:17], v[16:17], v[6:7] op_sel_hi:[1,1,0]
	v_fmamk_f32 v5, v78, 0xba000000, v5
	v_mul_f32_e32 v6, v8, v8
	v_pk_fma_f32 v[28:29], v[8:9], v[8:9], v[6:7] op_sel_hi:[1,1,0]
	v_fmamk_f32 v4, v78, 0xba000000, v4
	v_fmamk_f32 v3, v78, 0xba000000, v3
	v_fmac_f32_e32 v2, 0xba000000, v78
	v_mul_f32_e32 v6, v2, v2
	v_mul_f32_e32 v28, v3, v3
	v_mul_f32_e32 v70, v4, v4
	v_mul_f32_e32 v22, v5, v5
	v_pk_add_f32 v[6:7], v[6:7], v[28:29]
	v_pk_add_f32 v[22:23], v[70:71], v[22:23]
	s_nop 0
	v_pk_add_f32 v[6:7], v[6:7], v[22:23]
	s_nop 0
	v_add_f32_e32 v6, v6, v7
	ds_bpermute_b32 v7, v1, v6
	s_waitcnt lgkmcnt(0)
; __device__ __forceinline__ unsigned cvt_pk_bf16(float lo, float hi) { unsigned r; asm volatile("v_cvt_pk_bf16_f32 %0, %1, %2" : "=v"(r) : "v"(lo), "v"(hi)); return r; }
; __device__ __forceinline__ unsigned pk4_fp8(float a, float b, float c, float d) { int w = 0; w = __builtin_amdgcn_cvt_pk_fp8_f32(a, b, w, false); w = __builtin_amdgcn_cvt_pk_fp8_f32(c, d, w, true); return (unsigned)w; }
; __device__ __forceinline__ void p1_ln_mod(Frame& F) {
;     ...
;         const float mean = wave_sum(s) * (1.f / DM); float s2 = 0.f;
; #pragma unroll
;         for (int j = 0; j < 8; ++j) { v[j] = v[j] - mean; s2 += (v[j][0] * v[j][0] + v[j][1] * v[j][1]) + (v[j][2] * v[j][2] + v[j][3] * v[j][3]); }
;         const float rstd = 1.f / sqrtf(wave_sum(s2) * (1.f / DM) + LN_EPS);
;         u32x2* o8 = (u32x2*)((bf16_t*)(F.ws + WS_U) + (size_t)m * DM) + F.lane;
; #pragma unroll
;         for (int j = 0; j < 8; ++j) { const f32x4 sh = ((const f32x4*)md)[F.lane + 64 * j], sc = ((const f32x4*)(md + 2048))[F.lane + 64 * j];
;             const f32x4 y = v[j] * rstd * (sc + 1.0f) + sh; u32x2 w; w.x = cvt_pk_bf16(y[0], y[1]); w.y = cvt_pk_bf16(y[2], y[3]); o8[64 * j] = w;
;             ((unsigned*)(F.ws + WS_UF8 + (size_t)m * DM))[F.lane + 64 * j] = pk4_fp8(y[0], y[1], y[2], y[3]); }
	v_add_f32_e32 v6, v6, v7
	ds_bpermute_b32 v7, v42, v6
	s_waitcnt lgkmcnt(0)
	v_add_f32_e32 v6, v6, v7
	ds_bpermute_b32 v7, v43, v6
	s_waitcnt lgkmcnt(0)
	v_add_f32_e32 v6, v6, v7
	ds_bpermute_b32 v7, v44, v6
	s_waitcnt lgkmcnt(0)
	v_add_f32_e32 v6, v6, v7
	ds_bpermute_b32 v7, v45, v6
	s_waitcnt lgkmcnt(0)
	v_add_f32_e32 v6, v6, v7
	ds_bpermute_b32 v7, v46, v6
	s_waitcnt lgkmcnt(0)
	v_add_f32_e32 v6, v6, v7
	v_fmamk_f32 v6, v6, 0x3a000000, v47
	v_mul_f32_e32 v7, 0x4f800000, v6
	v_cmp_gt_f32_e32 vcc, s43, v6
	s_nop 1
	v_cndmask_b32_e32 v22, v6, v7, vcc
	v_sqrt_f32_e32 v23, v22
	v_lshl_add_u64 v[6:7], v[36:37], 0, s[0:1]
	v_add_u32_e32 v28, -1, v23
	v_add_u32_e32 v29, 1, v23
	v_fma_f32 v70, -v28, v23, v22
	v_fma_f32 v71, -v29, v23, v22
	v_cmp_ge_f32_e64 s[0:1], 0, v70
	s_nop 1
	v_cndmask_b32_e64 v23, v23, v28, s[0:1]
	v_cmp_lt_f32_e64 s[0:1], 0, v71
	s_nop 1
	v_cndmask_b32_e64 v23, v23, v29, s[0:1]
	v_mul_f32_e32 v28, 0x37800000, v23
	v_cndmask_b32_e32 v23, v23, v28, vcc
	v_cmp_class_f32_e32 vcc, v22, v48
	s_waitcnt vmcnt(0)
	v_pk_add_f32 v[28:29], v[60:61], 1.0 op_sel_hi:[1,0]
	v_cndmask_b32_e32 v22, v23, v22, vcc
	v_div_scale_f32 v23, s[0:1], v22, v22, 1.0
	v_rcp_f32_e32 v70, v23
	v_div_scale_f32 v60, vcc, 1.0, v22, 1.0
	v_fma_f32 v61, -v23, v70, 1.0
	v_fmac_f32_e32 v70, v61, v70
	v_mul_f32_e32 v61, v60, v70
	v_fma_f32 v71, -v23, v61, v60
	v_fmac_f32_e32 v61, v71, v70
	v_fma_f32 v23, -v23, v61, v60
	v_div_fmas_f32 v23, v23, v70, v61
	v_div_fixup_f32 v22, v23, v22, 1.0
	v_pk_mul_f32 v[30:31], v[30:31], v[22:23] op_sel_hi:[1,0]
	v_pk_mul_f32 v[32:33], v[32:33], v[22:23] op_sel_hi:[1,0]
	v_pk_fma_f32 v[28:29], v[28:29], v[30:31], v[56:57]
	v_mov_b32_e32 v23, 0
	v_cvt_pk_fp8_f32 v23, v28, v29
	v_pk_add_f32 v[30:31], v[62:63], 1.0 op_sel_hi:[1,0]
	v_cvt_pk_bf16_f32 v28, v28, v29
	s_nop 0
	v_pk_fma_f32 v[30:31], v[30:31], v[32:33], v[58:59]
	v_lshl_add_u64 v[32:33], v[38:39], 0, s[38:39]
	v_cvt_pk_fp8_f32 v23, v30, v31 op_sel:[0,0,1]
	v_cvt_pk_bf16_f32 v29, v30, v31
	global_store_dwordx2 v[6:7], v[28:29], off
	v_lshl_add_u64 v[28:29], v[40:41], 0, s[38:39]
	global_store_dword v[28:29], v23, off
	global_load_dwordx4 v[28:31], v49, s[24:25]
	s_nop 0
	global_load_dwordx4 v[56:59], v34, s[20:21] offset:1024
	v_mov_b32_e32 v23, 0
	v_pk_mul_f32 v[26:27], v[26:27], v[22:23] op_sel_hi:[1,0]
	v_add_co_u32_e32 v60, vcc, s44, v32
	s_waitcnt vmcnt(1)
	v_pk_add_f32 v[28:29], v[28:29], 1.0 op_sel_hi:[1,0]
	s_waitcnt vmcnt(0)
	v_pk_fma_f32 v[26:27], v[28:29], v[26:27], v[56:57]
	v_pk_add_f32 v[30:31], v[30:31], 1.0 op_sel_hi:[1,0]
	v_cvt_pk_fp8_f32 v23, v26, v27
	v_cvt_pk_bf16_f32 v26, v26, v27
	v_addc_co_u32_e32 v61, vcc, 0, v33, vcc
	v_pk_mul_f32 v[28:29], v[64:65], v[22:23] op_sel_hi:[1,0]
	s_nop 0
	v_pk_fma_f32 v[28:29], v[30:31], v[28:29], v[58:59]
	s_nop 0
	v_cvt_pk_fp8_f32 v23, v28, v29 op_sel:[0,0,1]
	v_cvt_pk_bf16_f32 v27, v28, v29
	global_store_dwordx2 v[6:7], v[26:27], off offset:512
	global_store_dword v[60:61], v23, off offset:256
	global_load_dwordx4 v[26:29], v50, s[24:25]
	s_nop 0
	global_load_dwordx4 v[30:33], v34, s[20:21] offset:2048
	v_mov_b32_e32 v23, 0
	v_pk_mul_f32 v[56:57], v[66:67], v[22:23] op_sel_hi:[1,0]
	s_waitcnt vmcnt(1)
	v_pk_add_f32 v[26:27], v[26:27], 1.0 op_sel_hi:[1,0]
	s_waitcnt vmcnt(0)
	v_pk_fma_f32 v[26:27], v[56:57], v[26:27], v[30:31]
	v_pk_add_f32 v[28:29], v[28:29], 1.0 op_sel_hi:[1,0]
	v_cvt_pk_fp8_f32 v23, v26, v27
	v_cvt_pk_bf16_f32 v26, v26, v27
	v_pk_mul_f32 v[24:25], v[24:25], v[22:23] op_sel_hi:[1,0]
	s_nop 0
	v_pk_fma_f32 v[24:25], v[24:25], v[28:29], v[32:33]
	s_nop 0
	v_cvt_pk_fp8_f32 v23, v24, v25 op_sel:[0,0,1]
	v_cvt_pk_bf16_f32 v27, v24, v25
	global_store_dwordx2 v[6:7], v[26:27], off offset:1024
	global_store_dword v[60:61], v23, off offset:512
	global_load_dwordx4 v[24:27], v51, s[24:25]
	s_nop 0
	global_load_dwordx4 v[28:31], v34, s[20:21] offset:3072
	v_mov_b32_e32 v23, 0
	v_pk_mul_f32 v[32:33], v[68:69], v[22:23] op_sel_hi:[1,0]
	s_waitcnt vmcnt(1)
; __device__ __forceinline__ unsigned cvt_pk_bf16(float lo, float hi) { unsigned r; asm volatile("v_cvt_pk_bf16_f32 %0, %1, %2" : "=v"(r) : "v"(lo), "v"(hi)); return r; }
; __device__ __forceinline__ unsigned pk4_fp8(float a, float b, float c, float d) { int w = 0; w = __builtin_amdgcn_cvt_pk_fp8_f32(a, b, w, false); w = __builtin_amdgcn_cvt_pk_fp8_f32(c, d, w, true); return (unsigned)w; }
; __device__ __forceinline__ void p1_ln_mod(Frame& F) {
;     ...
;         for (int j = 0; j < 8; ++j) { const f32x4 sh = ((const f32x4*)md)[F.lane + 64 * j], sc = ((const f32x4*)(md + 2048))[F.lane + 64 * j];
;             const f32x4 y = v[j] * rstd * (sc + 1.0f) + sh; u32x2 w; w.x = cvt_pk_bf16(y[0], y[1]); w.y = cvt_pk_bf16(y[2], y[3]); o8[64 * j] = w;
;             ((unsigned*)(F.ws + WS_UF8 + (size_t)m * DM))[F.lane + 64 * j] = pk4_fp8(y[0], y[1], y[2], y[3]); }
	v_pk_add_f32 v[24:25], v[24:25], 1.0 op_sel_hi:[1,0]
	s_waitcnt vmcnt(0)
	v_pk_fma_f32 v[24:25], v[32:33], v[24:25], v[28:29]
	v_pk_add_f32 v[26:27], v[26:27], 1.0 op_sel_hi:[1,0]
	v_cvt_pk_fp8_f32 v23, v24, v25
	v_cvt_pk_bf16_f32 v24, v24, v25
	v_pk_mul_f32 v[20:21], v[20:21], v[22:23] op_sel_hi:[1,0]
	s_nop 0
	v_pk_fma_f32 v[20:21], v[20:21], v[26:27], v[30:31]
	s_nop 0
	v_cvt_pk_fp8_f32 v23, v20, v21 op_sel:[0,0,1]
	v_cvt_pk_bf16_f32 v25, v20, v21
	global_store_dwordx2 v[6:7], v[24:25], off offset:1536
	global_store_dword v[60:61], v23, off offset:768
	global_load_dwordx4 v[24:27], v52, s[24:25]
	s_nop 0
	global_load_dwordx4 v[28:31], v52, s[20:21]
	v_mov_b32_e32 v23, 0
	v_pk_mul_f32 v[14:15], v[14:15], v[22:23] op_sel_hi:[1,0]
	s_waitcnt vmcnt(1)
	v_pk_add_f32 v[20:21], v[24:25], 1.0 op_sel_hi:[1,0]
	s_waitcnt vmcnt(0)
	v_pk_fma_f32 v[14:15], v[14:15], v[20:21], v[28:29]
	v_pk_add_f32 v[20:21], v[26:27], 1.0 op_sel_hi:[1,0]
	v_cvt_pk_fp8_f32 v23, v14, v15
	v_cvt_pk_bf16_f32 v14, v14, v15
	v_pk_mul_f32 v[18:19], v[18:19], v[22:23] op_sel_hi:[1,0]
	s_nop 0
	v_pk_fma_f32 v[18:19], v[18:19], v[20:21], v[30:31]
	s_nop 0
	v_cvt_pk_fp8_f32 v23, v18, v19 op_sel:[0,0,1]
	v_cvt_pk_bf16_f32 v15, v18, v19
	global_store_dwordx2 v[6:7], v[14:15], off offset:2048
	global_store_dword v[60:61], v23, off offset:1024
	global_load_dwordx4 v[18:21], v53, s[24:25]
	global_load_dwordx4 v[24:27], v53, s[20:21]
	v_mov_b32_e32 v23, 0
	v_pk_mul_f32 v[10:11], v[10:11], v[22:23] op_sel_hi:[1,0]
	s_waitcnt vmcnt(1)
	v_pk_add_f32 v[14:15], v[18:19], 1.0 op_sel_hi:[1,0]
	s_waitcnt vmcnt(0)
	v_pk_fma_f32 v[10:11], v[10:11], v[14:15], v[24:25]
	v_pk_add_f32 v[14:15], v[20:21], 1.0 op_sel_hi:[1,0]
	v_cvt_pk_fp8_f32 v23, v10, v11
	v_cvt_pk_bf16_f32 v10, v10, v11
	v_pk_mul_f32 v[12:13], v[12:13], v[22:23] op_sel_hi:[1,0]
	s_nop 0
	v_pk_fma_f32 v[12:13], v[12:13], v[14:15], v[26:27]
	s_nop 0
	v_cvt_pk_fp8_f32 v23, v12, v13 op_sel:[0,0,1]
	v_cvt_pk_bf16_f32 v11, v12, v13
	global_store_dwordx2 v[6:7], v[10:11], off offset:2560
	global_store_dword v[60:61], v23, off offset:1280
	global_load_dwordx4 v[10:13], v54, s[24:25]
	s_nop 0
	global_load_dwordx4 v[18:21], v54, s[20:21]
	v_mov_b32_e32 v23, 0
	v_pk_mul_f32 v[14:15], v[16:17], v[22:23] op_sel_hi:[1,0]
	s_waitcnt vmcnt(1)
	v_pk_add_f32 v[10:11], v[10:11], 1.0 op_sel_hi:[1,0]
	s_waitcnt vmcnt(0)
	v_pk_fma_f32 v[10:11], v[14:15], v[10:11], v[18:19]
	v_pk_add_f32 v[12:13], v[12:13], 1.0 op_sel_hi:[1,0]
	v_cvt_pk_fp8_f32 v23, v10, v11
	v_cvt_pk_bf16_f32 v10, v10, v11
	v_pk_mul_f32 v[8:9], v[8:9], v[22:23] op_sel_hi:[1,0]
	s_nop 0
	v_pk_fma_f32 v[8:9], v[8:9], v[12:13], v[20:21]
	s_nop 0
	v_cvt_pk_fp8_f32 v23, v8, v9 op_sel:[0,0,1]
	v_cvt_pk_bf16_f32 v11, v8, v9
	global_store_dwordx2 v[6:7], v[10:11], off offset:3072
	global_store_dword v[60:61], v23, off offset:1536
	global_load_dwordx4 v[8:11], v55, s[24:25]
	s_nop 0
	global_load_dwordx4 v[12:15], v55, s[20:21]
	v_pk_mul_f32 v[2:3], v[2:3], v[22:23] op_sel_hi:[1,0]
	v_pk_mul_f32 v[4:5], v[4:5], v[22:23] op_sel_hi:[1,0]
	s_waitcnt vmcnt(1)
	v_pk_add_f32 v[8:9], v[8:9], 1.0 op_sel_hi:[1,0]
	s_waitcnt vmcnt(0)
	v_pk_fma_f32 v[2:3], v[2:3], v[8:9], v[12:13]
	v_mov_b32_e32 v8, 0
	v_cvt_pk_fp8_f32 v8, v2, v3
	v_pk_add_f32 v[10:11], v[10:11], 1.0 op_sel_hi:[1,0]
	v_cvt_pk_bf16_f32 v2, v2, v3
	s_nop 0
	v_pk_fma_f32 v[4:5], v[4:5], v[10:11], v[14:15]
	s_nop 0
	v_cvt_pk_fp8_f32 v8, v4, v5 op_sel:[0,0,1]
	v_cvt_pk_bf16_f32 v3, v4, v5
	global_store_dwordx2 v[6:7], v[2:3], off offset:3584
	global_store_dword v[60:61], v8, off offset:1792
	s_cbranch_scc0 .LBB0_194
